# prologue: silu(c) staging loads and the rope-table position loads issued up front (no per-iteration wait behind the previous store)
# speedup vs baseline: 1.0135x; 1.0011x over previous
; __device__ __forceinline__ float siluf_(float x) { return x / (1.f + __expf(-x)); }
; __device__ __forceinline__ void p0_prologue(const Args& a, const int wv) {
;     ...
;         for (int i = F.tid; i < NBATCH * DM; i += 512) cs[i] = siluf_(a.c[i]);
.LBB0_8:
	s_cmp_lt_i32 s28, 1
	s_cselect_b64 s[2:3], -1, 0
	s_cmp_gt_i32 s29, 0
	s_cselect_b64 s[4:5], -1, 0
	s_and_b64 s[2:3], s[2:3], s[4:5]
	s_add_u32 s30, s0, 0x108
	s_addc_u32 s31, s1, 0
	s_and_b64 vcc, exec, s[2:3]
	s_cbranch_vccz .LBB0_161
	s_mov_b64 s[4:5], s[0:1]
	v_mbcnt_lo_u32_b32 v0, -1, 0
	v_mbcnt_hi_u32_b32 v0, -1, v0
	s_mov_b32 s10, s18
	v_or_b32_e32 v108, s19, v0
	s_load_dword s24, s[30:31], 0x0
	s_movk_i32 s2, 0x2000
	v_readfirstlane_b32 s25, v108
	v_cmp_gt_i32_e32 vcc, s2, v108
	v_ashrrev_i32_e32 v109, 31, v108
	s_waitcnt lgkmcnt(0)
	s_mov_b32 s8, s24
	s_load_dwordx2 s[6:7], s[4:5], 0xf8
	v_lshl_add_u32 v2, v108, 2, 0
	s_waitcnt lgkmcnt(0)
	s_and_saveexec_b64 s[2:3], vcc
	s_cbranch_execz .LBB0_12
	s_load_dwordx2 s[16:17], s[4:5], 0x8
	v_add_u32_e32 v3, 0xfffffe00, v108
	s_mov_b64 s[12:13], 0
	s_mov_b64 s[14:15], 0x800
	s_movk_i32 s9, 0x1dff
	s_waitcnt lgkmcnt(0)
	v_lshl_add_u64 v[0:1], v[108:109], 2, s[16:17]
	v_mov_b32_e32 v4, v2
	global_load_dword v32, v[0:1], off
	v_lshl_add_u64 v[0:1], v[0:1], 0, s[14:15]
	global_load_dword v33, v[0:1], off
	v_lshl_add_u64 v[0:1], v[0:1], 0, s[14:15]
	global_load_dword v34, v[0:1], off
	v_lshl_add_u64 v[0:1], v[0:1], 0, s[14:15]
	global_load_dword v35, v[0:1], off
	v_lshl_add_u64 v[0:1], v[0:1], 0, s[14:15]
	global_load_dword v36, v[0:1], off
	v_lshl_add_u64 v[0:1], v[0:1], 0, s[14:15]
	global_load_dword v37, v[0:1], off
	v_lshl_add_u64 v[0:1], v[0:1], 0, s[14:15]
	global_load_dword v38, v[0:1], off
	v_lshl_add_u64 v[0:1], v[0:1], 0, s[14:15]
	global_load_dword v39, v[0:1], off
	v_lshl_add_u64 v[0:1], v[0:1], 0, s[14:15]
	global_load_dword v40, v[0:1], off
	v_lshl_add_u64 v[0:1], v[0:1], 0, s[14:15]
	global_load_dword v41, v[0:1], off
	v_lshl_add_u64 v[0:1], v[0:1], 0, s[14:15]
	global_load_dword v42, v[0:1], off
	v_lshl_add_u64 v[0:1], v[0:1], 0, s[14:15]
	global_load_dword v43, v[0:1], off
	v_lshl_add_u64 v[0:1], v[0:1], 0, s[14:15]
	global_load_dword v44, v[0:1], off
	v_lshl_add_u64 v[0:1], v[0:1], 0, s[14:15]
	global_load_dword v45, v[0:1], off
	v_lshl_add_u64 v[0:1], v[0:1], 0, s[14:15]
	global_load_dword v46, v[0:1], off
	v_lshl_add_u64 v[0:1], v[0:1], 0, s[14:15]
	global_load_dword v47, v[0:1], off
	s_waitcnt vmcnt(15)
	v_mul_f32_e32 v6, 0xbfb8aa3b, v32
	v_exp_f32_e32 v6, v6
	s_nop 0
	v_add_f32_e32 v6, 1.0, v6
	v_div_scale_f32 v7, s[16:17], v6, v6, v32
	v_rcp_f32_e32 v8, v7
	v_div_scale_f32 v9, vcc, v32, v6, v32
	v_fma_f32 v10, -v7, v8, 1.0
	v_fmac_f32_e32 v8, v10, v8
	v_mul_f32_e32 v10, v9, v8
	v_fma_f32 v11, -v7, v10, v9
	v_fmac_f32_e32 v10, v11, v8
	v_fma_f32 v7, -v7, v10, v9
	v_div_fmas_f32 v7, v7, v8, v10
	v_div_fixup_f32 v5, v7, v6, v32
	ds_write_b32 v4, v5
	s_waitcnt vmcnt(14)
	v_mul_f32_e32 v6, 0xbfb8aa3b, v33
	v_exp_f32_e32 v6, v6
	s_nop 0
	v_add_f32_e32 v6, 1.0, v6
	v_div_scale_f32 v7, s[16:17], v6, v6, v33
	v_rcp_f32_e32 v8, v7
	v_div_scale_f32 v9, vcc, v33, v6, v33
	v_fma_f32 v10, -v7, v8, 1.0
	v_fmac_f32_e32 v8, v10, v8
	v_mul_f32_e32 v10, v9, v8
	v_fma_f32 v11, -v7, v10, v9
	v_fmac_f32_e32 v10, v11, v8
	v_fma_f32 v7, -v7, v10, v9
	v_div_fmas_f32 v7, v7, v8, v10
	v_div_fixup_f32 v5, v7, v6, v33
	ds_write_b32 v4, v5 offset:2048
	s_waitcnt vmcnt(13)
	v_mul_f32_e32 v6, 0xbfb8aa3b, v34
	v_exp_f32_e32 v6, v6
	s_nop 0
	v_add_f32_e32 v6, 1.0, v6
	v_div_scale_f32 v7, s[16:17], v6, v6, v34
	v_rcp_f32_e32 v8, v7
	v_div_scale_f32 v9, vcc, v34, v6, v34
	v_fma_f32 v10, -v7, v8, 1.0
	v_fmac_f32_e32 v8, v10, v8
	v_mul_f32_e32 v10, v9, v8
	v_fma_f32 v11, -v7, v10, v9
	v_fmac_f32_e32 v10, v11, v8
	v_fma_f32 v7, -v7, v10, v9
	v_div_fmas_f32 v7, v7, v8, v10
	v_div_fixup_f32 v5, v7, v6, v34
	ds_write_b32 v4, v5 offset:4096
	s_waitcnt vmcnt(12)
	v_mul_f32_e32 v6, 0xbfb8aa3b, v35
	v_exp_f32_e32 v6, v6
	s_nop 0
	v_add_f32_e32 v6, 1.0, v6
	v_div_scale_f32 v7, s[16:17], v6, v6, v35
	v_rcp_f32_e32 v8, v7
	v_div_scale_f32 v9, vcc, v35, v6, v35
	v_fma_f32 v10, -v7, v8, 1.0
	v_fmac_f32_e32 v8, v10, v8
	v_mul_f32_e32 v10, v9, v8
	v_fma_f32 v11, -v7, v10, v9
	v_fmac_f32_e32 v10, v11, v8
	v_fma_f32 v7, -v7, v10, v9
	v_div_fmas_f32 v7, v7, v8, v10
	v_div_fixup_f32 v5, v7, v6, v35
	ds_write_b32 v4, v5 offset:6144
	s_waitcnt vmcnt(11)
	v_mul_f32_e32 v6, 0xbfb8aa3b, v36
	v_exp_f32_e32 v6, v6
	s_nop 0
	v_add_f32_e32 v6, 1.0, v6
	v_div_scale_f32 v7, s[16:17], v6, v6, v36
	v_rcp_f32_e32 v8, v7
	v_div_scale_f32 v9, vcc, v36, v6, v36
	v_fma_f32 v10, -v7, v8, 1.0
	v_fmac_f32_e32 v8, v10, v8
	v_mul_f32_e32 v10, v9, v8
	v_fma_f32 v11, -v7, v10, v9
	v_fmac_f32_e32 v10, v11, v8
	v_fma_f32 v7, -v7, v10, v9
	v_div_fmas_f32 v7, v7, v8, v10
	v_div_fixup_f32 v5, v7, v6, v36
	ds_write_b32 v4, v5 offset:8192
	s_waitcnt vmcnt(10)
	v_mul_f32_e32 v6, 0xbfb8aa3b, v37
	v_exp_f32_e32 v6, v6
	s_nop 0
	v_add_f32_e32 v6, 1.0, v6
	v_div_scale_f32 v7, s[16:17], v6, v6, v37
	v_rcp_f32_e32 v8, v7
	v_div_scale_f32 v9, vcc, v37, v6, v37
	v_fma_f32 v10, -v7, v8, 1.0
	v_fmac_f32_e32 v8, v10, v8
	v_mul_f32_e32 v10, v9, v8
	v_fma_f32 v11, -v7, v10, v9
	v_fmac_f32_e32 v10, v11, v8
	v_fma_f32 v7, -v7, v10, v9
	v_div_fmas_f32 v7, v7, v8, v10
	v_div_fixup_f32 v5, v7, v6, v37
	ds_write_b32 v4, v5 offset:10240
	s_waitcnt vmcnt(9)
; __device__ __forceinline__ float siluf_(float x) { return x / (1.f + __expf(-x)); }
; __device__ __forceinline__ void p0_prologue(const Args& a, const int wv) {
;     ...
;         for (int i = F.tid; i < NBATCH * DM; i += 512) cs[i] = siluf_(a.c[i]);
	v_mul_f32_e32 v6, 0xbfb8aa3b, v38
	v_exp_f32_e32 v6, v6
	s_nop 0
	v_add_f32_e32 v6, 1.0, v6
	v_div_scale_f32 v7, s[16:17], v6, v6, v38
	v_rcp_f32_e32 v8, v7
	v_div_scale_f32 v9, vcc, v38, v6, v38
	v_fma_f32 v10, -v7, v8, 1.0
	v_fmac_f32_e32 v8, v10, v8
	v_mul_f32_e32 v10, v9, v8
	v_fma_f32 v11, -v7, v10, v9
	v_fmac_f32_e32 v10, v11, v8
	v_fma_f32 v7, -v7, v10, v9
	v_div_fmas_f32 v7, v7, v8, v10
	v_div_fixup_f32 v5, v7, v6, v38
	ds_write_b32 v4, v5 offset:12288
	s_waitcnt vmcnt(8)
	v_mul_f32_e32 v6, 0xbfb8aa3b, v39
	v_exp_f32_e32 v6, v6
	s_nop 0
	v_add_f32_e32 v6, 1.0, v6
	v_div_scale_f32 v7, s[16:17], v6, v6, v39
	v_rcp_f32_e32 v8, v7
	v_div_scale_f32 v9, vcc, v39, v6, v39
	v_fma_f32 v10, -v7, v8, 1.0
	v_fmac_f32_e32 v8, v10, v8
	v_mul_f32_e32 v10, v9, v8
	v_fma_f32 v11, -v7, v10, v9
	v_fmac_f32_e32 v10, v11, v8
	v_fma_f32 v7, -v7, v10, v9
	v_div_fmas_f32 v7, v7, v8, v10
	v_div_fixup_f32 v5, v7, v6, v39
	ds_write_b32 v4, v5 offset:14336
	s_waitcnt vmcnt(7)
	v_mul_f32_e32 v6, 0xbfb8aa3b, v40
	v_exp_f32_e32 v6, v6
	s_nop 0
	v_add_f32_e32 v6, 1.0, v6
	v_div_scale_f32 v7, s[16:17], v6, v6, v40
	v_rcp_f32_e32 v8, v7
	v_div_scale_f32 v9, vcc, v40, v6, v40
	v_fma_f32 v10, -v7, v8, 1.0
	v_fmac_f32_e32 v8, v10, v8
	v_mul_f32_e32 v10, v9, v8
	v_fma_f32 v11, -v7, v10, v9
	v_fmac_f32_e32 v10, v11, v8
	v_fma_f32 v7, -v7, v10, v9
	v_div_fmas_f32 v7, v7, v8, v10
	v_div_fixup_f32 v5, v7, v6, v40
	ds_write_b32 v4, v5 offset:16384
	s_waitcnt vmcnt(6)
	v_mul_f32_e32 v6, 0xbfb8aa3b, v41
	v_exp_f32_e32 v6, v6
	s_nop 0
	v_add_f32_e32 v6, 1.0, v6
	v_div_scale_f32 v7, s[16:17], v6, v6, v41
	v_rcp_f32_e32 v8, v7
	v_div_scale_f32 v9, vcc, v41, v6, v41
	v_fma_f32 v10, -v7, v8, 1.0
	v_fmac_f32_e32 v8, v10, v8
	v_mul_f32_e32 v10, v9, v8
	v_fma_f32 v11, -v7, v10, v9
	v_fmac_f32_e32 v10, v11, v8
	v_fma_f32 v7, -v7, v10, v9
	v_div_fmas_f32 v7, v7, v8, v10
	v_div_fixup_f32 v5, v7, v6, v41
	ds_write_b32 v4, v5 offset:18432
	s_waitcnt vmcnt(5)
	v_mul_f32_e32 v6, 0xbfb8aa3b, v42
	v_exp_f32_e32 v6, v6
	s_nop 0
	v_add_f32_e32 v6, 1.0, v6
	v_div_scale_f32 v7, s[16:17], v6, v6, v42
	v_rcp_f32_e32 v8, v7
	v_div_scale_f32 v9, vcc, v42, v6, v42
	v_fma_f32 v10, -v7, v8, 1.0
	v_fmac_f32_e32 v8, v10, v8
	v_mul_f32_e32 v10, v9, v8
	v_fma_f32 v11, -v7, v10, v9
	v_fmac_f32_e32 v10, v11, v8
	v_fma_f32 v7, -v7, v10, v9
	v_div_fmas_f32 v7, v7, v8, v10
	v_div_fixup_f32 v5, v7, v6, v42
	ds_write_b32 v4, v5 offset:20480
	s_waitcnt vmcnt(4)
	v_mul_f32_e32 v6, 0xbfb8aa3b, v43
	v_exp_f32_e32 v6, v6
	s_nop 0
	v_add_f32_e32 v6, 1.0, v6
	v_div_scale_f32 v7, s[16:17], v6, v6, v43
	v_rcp_f32_e32 v8, v7
	v_div_scale_f32 v9, vcc, v43, v6, v43
	v_fma_f32 v10, -v7, v8, 1.0
	v_fmac_f32_e32 v8, v10, v8
	v_mul_f32_e32 v10, v9, v8
	v_fma_f32 v11, -v7, v10, v9
	v_fmac_f32_e32 v10, v11, v8
	v_fma_f32 v7, -v7, v10, v9
	v_div_fmas_f32 v7, v7, v8, v10
	v_div_fixup_f32 v5, v7, v6, v43
	ds_write_b32 v4, v5 offset:22528
	s_waitcnt vmcnt(3)
	v_mul_f32_e32 v6, 0xbfb8aa3b, v44
	v_exp_f32_e32 v6, v6
	s_nop 0
	v_add_f32_e32 v6, 1.0, v6
	v_div_scale_f32 v7, s[16:17], v6, v6, v44
	v_rcp_f32_e32 v8, v7
	v_div_scale_f32 v9, vcc, v44, v6, v44
	v_fma_f32 v10, -v7, v8, 1.0
	v_fmac_f32_e32 v8, v10, v8
	v_mul_f32_e32 v10, v9, v8
	v_fma_f32 v11, -v7, v10, v9
	v_fmac_f32_e32 v10, v11, v8
	v_fma_f32 v7, -v7, v10, v9
	v_div_fmas_f32 v7, v7, v8, v10
	v_div_fixup_f32 v5, v7, v6, v44
	ds_write_b32 v4, v5 offset:24576
	s_waitcnt vmcnt(2)
	v_mul_f32_e32 v6, 0xbfb8aa3b, v45
	v_exp_f32_e32 v6, v6
	s_nop 0
	v_add_f32_e32 v6, 1.0, v6
	v_div_scale_f32 v7, s[16:17], v6, v6, v45
	v_rcp_f32_e32 v8, v7
	v_div_scale_f32 v9, vcc, v45, v6, v45
	v_fma_f32 v10, -v7, v8, 1.0
	v_fmac_f32_e32 v8, v10, v8
	v_mul_f32_e32 v10, v9, v8
	v_fma_f32 v11, -v7, v10, v9
	v_fmac_f32_e32 v10, v11, v8
	v_fma_f32 v7, -v7, v10, v9
	v_div_fmas_f32 v7, v7, v8, v10
	v_div_fixup_f32 v5, v7, v6, v45
	ds_write_b32 v4, v5 offset:26624
	s_waitcnt vmcnt(1)
	v_mul_f32_e32 v6, 0xbfb8aa3b, v46
	v_exp_f32_e32 v6, v6
	s_nop 0
	v_add_f32_e32 v6, 1.0, v6
	v_div_scale_f32 v7, s[16:17], v6, v6, v46
	v_rcp_f32_e32 v8, v7
	v_div_scale_f32 v9, vcc, v46, v6, v46
	v_fma_f32 v10, -v7, v8, 1.0
	v_fmac_f32_e32 v8, v10, v8
	v_mul_f32_e32 v10, v9, v8
	v_fma_f32 v11, -v7, v10, v9
	v_fmac_f32_e32 v10, v11, v8
	v_fma_f32 v7, -v7, v10, v9
	v_div_fmas_f32 v7, v7, v8, v10
	v_div_fixup_f32 v5, v7, v6, v46
	ds_write_b32 v4, v5 offset:28672
	s_waitcnt vmcnt(0)
	v_mul_f32_e32 v6, 0xbfb8aa3b, v47
	v_exp_f32_e32 v6, v6
	s_nop 0
	v_add_f32_e32 v6, 1.0, v6
	v_div_scale_f32 v7, s[16:17], v6, v6, v47
	v_rcp_f32_e32 v8, v7
	v_div_scale_f32 v9, vcc, v47, v6, v47
	v_fma_f32 v10, -v7, v8, 1.0
	v_fmac_f32_e32 v8, v10, v8
	v_mul_f32_e32 v10, v9, v8
	v_fma_f32 v11, -v7, v10, v9
	v_fmac_f32_e32 v10, v11, v8
	v_fma_f32 v7, -v7, v10, v9
	v_div_fmas_f32 v7, v7, v8, v10
	v_div_fixup_f32 v5, v7, v6, v47
	ds_write_b32 v4, v5 offset:30720

; __device__ __forceinline__ void p0_prologue(const Args& a, const int wv) {
;     ...
;         { const int f = (int)(gt & 127); const float invr = exp2f(-(float)(2 * f) * (13.287712379549449f / 256.f)) * 0.15915494309189535f;
;           for (size_t i = gt; i < (size_t)NTOK * 128; i += GT) { const int tok = (int)(i >> 7); float rv = __builtin_amdgcn_fractf((float)a.pos[tok] * invr);
;               unsigned pk_;
;               asm volatile("v_cos_f32 %0, %1\n\tv_sin_f32 %1, %1\n\ts_nop 1\n\tv_cvt_pk_bf16_f32 %0, %0, %1" : "=&v"(pk_), "+v"(rv)); ro[i] = pk_; } }
.LBB0_20:
	s_ashr_i32 s11, s10, 31
	s_lshl_b64 s[2:3], s[10:11], 9
	v_lshl_add_u64 v[0:1], s[2:3], 0, v[108:109]
	s_ashr_i32 s9, s8, 31
	s_mov_b64 s[12:13], 0x400000
	s_lshl_b64 s[2:3], s[8:9], 9
	v_lshlrev_b32_e32 v6, 1, v108
	v_cmp_gt_u64_e32 vcc, s[12:13], v[0:1]
	s_barrier
	s_and_saveexec_b64 s[12:13], vcc
	s_cbranch_execz .LBB0_23
	v_and_b32_e32 v2, 0xfe, v6
	v_cvt_f32_ubyte0_e32 v2, v2
	v_mul_f32_e32 v3, 0xbd549a78, v2
	s_mov_b32 s14, 0xc2fc0000
	v_mov_b32_e32 v4, 0x42800000
	v_cmp_gt_f32_e32 vcc, s14, v3
	s_load_dwordx2 s[14:15], s[4:5], 0x10
	s_lshl_b64 s[16:17], s[10:11], 11
	v_cndmask_b32_e32 v3, 0, v4, vcc
	v_fmac_f32_e32 v3, 0xbd549a78, v2
	v_exp_f32_e32 v2, v3
	v_not_b32_e32 v3, 63
	v_cndmask_b32_e32 v3, 0, v3, vcc
	s_add_u32 s16, s6, s16
	v_ldexp_f32 v2, v2, v3
	s_addc_u32 s17, s7, s17
	v_mul_f32_e32 v7, 0.15915494, v2
	v_lshl_add_u64 v[2:3], v[108:109], 2, s[16:17]
	s_mov_b64 s[16:17], 0x800000
	v_lshl_add_u64 v[2:3], v[2:3], 0, s[16:17]
	s_lshl_b64 s[16:17], s[8:9], 11
	s_mov_b64 s[20:21], 0
	s_mov_b64 s[22:23], 0x3fffff
	v_mov_b64_e32 v[4:5], v[0:1]
	s_cmp_lg_u32 s8, 0x100
	s_cbranch_scc1 .LBB0_22
	s_mov_b32 s20, 0x1000
	s_mov_b32 s21, 0
	v_lshrrev_b64 v[8:9], 5, v[4:5]
	v_and_b32_e32 v8, -4, v8
	s_waitcnt lgkmcnt(0)
	v_lshl_add_u64 v[8:9], s[14:15], 0, v[8:9]
	global_load_dword v16, v[8:9], off
	v_lshl_add_u64 v[8:9], v[8:9], 0, s[20:21]
	global_load_dword v17, v[8:9], off
	v_lshl_add_u64 v[8:9], v[8:9], 0, s[20:21]
	global_load_dword v18, v[8:9], off
	v_lshl_add_u64 v[8:9], v[8:9], 0, s[20:21]
	global_load_dword v19, v[8:9], off
	v_lshl_add_u64 v[8:9], v[8:9], 0, s[20:21]
	global_load_dword v20, v[8:9], off
	v_lshl_add_u64 v[8:9], v[8:9], 0, s[20:21]
	global_load_dword v21, v[8:9], off
	v_lshl_add_u64 v[8:9], v[8:9], 0, s[20:21]
	global_load_dword v22, v[8:9], off
	v_lshl_add_u64 v[8:9], v[8:9], 0, s[20:21]
	global_load_dword v23, v[8:9], off
	v_lshl_add_u64 v[8:9], v[8:9], 0, s[20:21]
	global_load_dword v24, v[8:9], off
	v_lshl_add_u64 v[8:9], v[8:9], 0, s[20:21]
	global_load_dword v25, v[8:9], off
	v_lshl_add_u64 v[8:9], v[8:9], 0, s[20:21]
	global_load_dword v26, v[8:9], off
	v_lshl_add_u64 v[8:9], v[8:9], 0, s[20:21]
	global_load_dword v27, v[8:9], off
	v_lshl_add_u64 v[8:9], v[8:9], 0, s[20:21]
	global_load_dword v28, v[8:9], off
	v_lshl_add_u64 v[8:9], v[8:9], 0, s[20:21]
	global_load_dword v29, v[8:9], off
	v_lshl_add_u64 v[8:9], v[8:9], 0, s[20:21]
	global_load_dword v30, v[8:9], off
	v_lshl_add_u64 v[8:9], v[8:9], 0, s[20:21]
	global_load_dword v31, v[8:9], off
	v_lshl_add_u64 v[8:9], v[8:9], 0, s[20:21]
	global_load_dword v32, v[8:9], off
	v_lshl_add_u64 v[8:9], v[8:9], 0, s[20:21]
	global_load_dword v33, v[8:9], off
	v_lshl_add_u64 v[8:9], v[8:9], 0, s[20:21]
	global_load_dword v34, v[8:9], off
	v_lshl_add_u64 v[8:9], v[8:9], 0, s[20:21]
	global_load_dword v35, v[8:9], off
	v_lshl_add_u64 v[8:9], v[8:9], 0, s[20:21]
	global_load_dword v36, v[8:9], off
	v_lshl_add_u64 v[8:9], v[8:9], 0, s[20:21]
	global_load_dword v37, v[8:9], off
	v_lshl_add_u64 v[8:9], v[8:9], 0, s[20:21]
	global_load_dword v38, v[8:9], off
	v_lshl_add_u64 v[8:9], v[8:9], 0, s[20:21]
	global_load_dword v39, v[8:9], off
	v_lshl_add_u64 v[8:9], v[8:9], 0, s[20:21]
	global_load_dword v40, v[8:9], off
	v_lshl_add_u64 v[8:9], v[8:9], 0, s[20:21]
	global_load_dword v41, v[8:9], off
	v_lshl_add_u64 v[8:9], v[8:9], 0, s[20:21]
	global_load_dword v42, v[8:9], off
	v_lshl_add_u64 v[8:9], v[8:9], 0, s[20:21]
	global_load_dword v43, v[8:9], off
	v_lshl_add_u64 v[8:9], v[8:9], 0, s[20:21]
	global_load_dword v44, v[8:9], off
	v_lshl_add_u64 v[8:9], v[8:9], 0, s[20:21]
	global_load_dword v45, v[8:9], off
	v_lshl_add_u64 v[8:9], v[8:9], 0, s[20:21]
	global_load_dword v46, v[8:9], off
	v_lshl_add_u64 v[8:9], v[8:9], 0, s[20:21]
	global_load_dword v47, v[8:9], off
	s_waitcnt vmcnt(31)
	v_cvt_f32_i32_e32 v10, v16
	v_mul_f32_e32 v10, v7, v10
	v_fract_f32_e32 v10, v10
	v_cos_f32 v11, v10
	v_sin_f32 v10, v10
	s_nop 1
	v_cvt_pk_bf16_f32 v11, v11, v10
	global_store_dword v[2:3], v11, off
	v_lshl_add_u64 v[2:3], v[2:3], 0, s[16:17]
	s_waitcnt vmcnt(31)
	v_cvt_f32_i32_e32 v10, v17
	v_mul_f32_e32 v10, v7, v10
	v_fract_f32_e32 v10, v10
	v_cos_f32 v11, v10
	v_sin_f32 v10, v10
	s_nop 1
	v_cvt_pk_bf16_f32 v11, v11, v10
	global_store_dword v[2:3], v11, off
	v_lshl_add_u64 v[2:3], v[2:3], 0, s[16:17]
	s_waitcnt vmcnt(31)
	v_cvt_f32_i32_e32 v10, v18
	v_mul_f32_e32 v10, v7, v10
	v_fract_f32_e32 v10, v10
	v_cos_f32 v11, v10
	v_sin_f32 v10, v10
	s_nop 1
	v_cvt_pk_bf16_f32 v11, v11, v10
	global_store_dword v[2:3], v11, off
	v_lshl_add_u64 v[2:3], v[2:3], 0, s[16:17]
	s_waitcnt vmcnt(31)
	v_cvt_f32_i32_e32 v10, v19
	v_mul_f32_e32 v10, v7, v10
	v_fract_f32_e32 v10, v10
	v_cos_f32 v11, v10
	v_sin_f32 v10, v10
	s_nop 1
	v_cvt_pk_bf16_f32 v11, v11, v10
	global_store_dword v[2:3], v11, off
	v_lshl_add_u64 v[2:3], v[2:3], 0, s[16:17]
	s_waitcnt vmcnt(31)
	v_cvt_f32_i32_e32 v10, v20
	v_mul_f32_e32 v10, v7, v10
	v_fract_f32_e32 v10, v10
	v_cos_f32 v11, v10
	v_sin_f32 v10, v10
	s_nop 1
	v_cvt_pk_bf16_f32 v11, v11, v10
	global_store_dword v[2:3], v11, off
	v_lshl_add_u64 v[2:3], v[2:3], 0, s[16:17]
	s_waitcnt vmcnt(31)
	v_cvt_f32_i32_e32 v10, v21
	v_mul_f32_e32 v10, v7, v10
	v_fract_f32_e32 v10, v10
	v_cos_f32 v11, v10
	v_sin_f32 v10, v10
	s_nop 1
	v_cvt_pk_bf16_f32 v11, v11, v10
	global_store_dword v[2:3], v11, off
	v_lshl_add_u64 v[2:3], v[2:3], 0, s[16:17]
	s_waitcnt vmcnt(31)
	v_cvt_f32_i32_e32 v10, v22
	v_mul_f32_e32 v10, v7, v10
	v_fract_f32_e32 v10, v10
	v_cos_f32 v11, v10
	v_sin_f32 v10, v10
	s_nop 1
	v_cvt_pk_bf16_f32 v11, v11, v10
	global_store_dword v[2:3], v11, off
	v_lshl_add_u64 v[2:3], v[2:3], 0, s[16:17]
	s_waitcnt vmcnt(31)
; __device__ __forceinline__ void p0_prologue(const Args& a, const int wv) {
;     ...
;         { const int f = (int)(gt & 127); const float invr = exp2f(-(float)(2 * f) * (13.287712379549449f / 256.f)) * 0.15915494309189535f;
;           for (size_t i = gt; i < (size_t)NTOK * 128; i += GT) { const int tok = (int)(i >> 7); float rv = __builtin_amdgcn_fractf((float)a.pos[tok] * invr);
;               unsigned pk_;
;               asm volatile("v_cos_f32 %0, %1\n\tv_sin_f32 %1, %1\n\ts_nop 1\n\tv_cvt_pk_bf16_f32 %0, %0, %1" : "=&v"(pk_), "+v"(rv)); ro[i] = pk_; } }
	v_cvt_f32_i32_e32 v10, v23
	v_mul_f32_e32 v10, v7, v10
	v_fract_f32_e32 v10, v10
	v_cos_f32 v11, v10
	v_sin_f32 v10, v10
	s_nop 1
	v_cvt_pk_bf16_f32 v11, v11, v10
	global_store_dword v[2:3], v11, off
	v_lshl_add_u64 v[2:3], v[2:3], 0, s[16:17]
	s_waitcnt vmcnt(31)
	v_cvt_f32_i32_e32 v10, v24
	v_mul_f32_e32 v10, v7, v10
	v_fract_f32_e32 v10, v10
	v_cos_f32 v11, v10
	v_sin_f32 v10, v10
	s_nop 1
	v_cvt_pk_bf16_f32 v11, v11, v10
	global_store_dword v[2:3], v11, off
	v_lshl_add_u64 v[2:3], v[2:3], 0, s[16:17]
	s_waitcnt vmcnt(31)
	v_cvt_f32_i32_e32 v10, v25
	v_mul_f32_e32 v10, v7, v10
	v_fract_f32_e32 v10, v10
	v_cos_f32 v11, v10
	v_sin_f32 v10, v10
	s_nop 1
	v_cvt_pk_bf16_f32 v11, v11, v10
	global_store_dword v[2:3], v11, off
	v_lshl_add_u64 v[2:3], v[2:3], 0, s[16:17]
	s_waitcnt vmcnt(31)
	v_cvt_f32_i32_e32 v10, v26
	v_mul_f32_e32 v10, v7, v10
	v_fract_f32_e32 v10, v10
	v_cos_f32 v11, v10
	v_sin_f32 v10, v10
	s_nop 1
	v_cvt_pk_bf16_f32 v11, v11, v10
	global_store_dword v[2:3], v11, off
	v_lshl_add_u64 v[2:3], v[2:3], 0, s[16:17]
	s_waitcnt vmcnt(31)
	v_cvt_f32_i32_e32 v10, v27
	v_mul_f32_e32 v10, v7, v10
	v_fract_f32_e32 v10, v10
	v_cos_f32 v11, v10
	v_sin_f32 v10, v10
	s_nop 1
	v_cvt_pk_bf16_f32 v11, v11, v10
	global_store_dword v[2:3], v11, off
	v_lshl_add_u64 v[2:3], v[2:3], 0, s[16:17]
	s_waitcnt vmcnt(31)
	v_cvt_f32_i32_e32 v10, v28
	v_mul_f32_e32 v10, v7, v10
	v_fract_f32_e32 v10, v10
	v_cos_f32 v11, v10
	v_sin_f32 v10, v10
	s_nop 1
	v_cvt_pk_bf16_f32 v11, v11, v10
	global_store_dword v[2:3], v11, off
	v_lshl_add_u64 v[2:3], v[2:3], 0, s[16:17]
	s_waitcnt vmcnt(31)
	v_cvt_f32_i32_e32 v10, v29
	v_mul_f32_e32 v10, v7, v10
	v_fract_f32_e32 v10, v10
	v_cos_f32 v11, v10
	v_sin_f32 v10, v10
	s_nop 1
	v_cvt_pk_bf16_f32 v11, v11, v10
	global_store_dword v[2:3], v11, off
	v_lshl_add_u64 v[2:3], v[2:3], 0, s[16:17]
	s_waitcnt vmcnt(31)
	v_cvt_f32_i32_e32 v10, v30
	v_mul_f32_e32 v10, v7, v10
	v_fract_f32_e32 v10, v10
	v_cos_f32 v11, v10
	v_sin_f32 v10, v10
	s_nop 1
	v_cvt_pk_bf16_f32 v11, v11, v10
	global_store_dword v[2:3], v11, off
	v_lshl_add_u64 v[2:3], v[2:3], 0, s[16:17]
	s_waitcnt vmcnt(31)
	v_cvt_f32_i32_e32 v10, v31
	v_mul_f32_e32 v10, v7, v10
	v_fract_f32_e32 v10, v10
	v_cos_f32 v11, v10
	v_sin_f32 v10, v10
	s_nop 1
	v_cvt_pk_bf16_f32 v11, v11, v10
	global_store_dword v[2:3], v11, off
	v_lshl_add_u64 v[2:3], v[2:3], 0, s[16:17]
	s_waitcnt vmcnt(31)
	v_cvt_f32_i32_e32 v10, v32
	v_mul_f32_e32 v10, v7, v10
	v_fract_f32_e32 v10, v10
	v_cos_f32 v11, v10
	v_sin_f32 v10, v10
	s_nop 1
	v_cvt_pk_bf16_f32 v11, v11, v10
	global_store_dword v[2:3], v11, off
	v_lshl_add_u64 v[2:3], v[2:3], 0, s[16:17]
	s_waitcnt vmcnt(31)
	v_cvt_f32_i32_e32 v10, v33
	v_mul_f32_e32 v10, v7, v10
	v_fract_f32_e32 v10, v10
	v_cos_f32 v11, v10
	v_sin_f32 v10, v10
	s_nop 1
	v_cvt_pk_bf16_f32 v11, v11, v10
	global_store_dword v[2:3], v11, off
	v_lshl_add_u64 v[2:3], v[2:3], 0, s[16:17]
	s_waitcnt vmcnt(31)
	v_cvt_f32_i32_e32 v10, v34
	v_mul_f32_e32 v10, v7, v10
	v_fract_f32_e32 v10, v10
	v_cos_f32 v11, v10
	v_sin_f32 v10, v10
	s_nop 1
	v_cvt_pk_bf16_f32 v11, v11, v10
	global_store_dword v[2:3], v11, off
	v_lshl_add_u64 v[2:3], v[2:3], 0, s[16:17]
	s_waitcnt vmcnt(31)
	v_cvt_f32_i32_e32 v10, v35
	v_mul_f32_e32 v10, v7, v10
	v_fract_f32_e32 v10, v10
	v_cos_f32 v11, v10
	v_sin_f32 v10, v10
	s_nop 1
	v_cvt_pk_bf16_f32 v11, v11, v10
	global_store_dword v[2:3], v11, off
	v_lshl_add_u64 v[2:3], v[2:3], 0, s[16:17]
	s_waitcnt vmcnt(31)
	v_cvt_f32_i32_e32 v10, v36
	v_mul_f32_e32 v10, v7, v10
	v_fract_f32_e32 v10, v10
	v_cos_f32 v11, v10
	v_sin_f32 v10, v10
	s_nop 1
	v_cvt_pk_bf16_f32 v11, v11, v10
	global_store_dword v[2:3], v11, off
	v_lshl_add_u64 v[2:3], v[2:3], 0, s[16:17]
	s_waitcnt vmcnt(31)
	v_cvt_f32_i32_e32 v10, v37
	v_mul_f32_e32 v10, v7, v10
	v_fract_f32_e32 v10, v10
	v_cos_f32 v11, v10
	v_sin_f32 v10, v10
	s_nop 1
	v_cvt_pk_bf16_f32 v11, v11, v10
	global_store_dword v[2:3], v11, off
	v_lshl_add_u64 v[2:3], v[2:3], 0, s[16:17]
	s_waitcnt vmcnt(31)
	v_cvt_f32_i32_e32 v10, v38
	v_mul_f32_e32 v10, v7, v10
	v_fract_f32_e32 v10, v10
	v_cos_f32 v11, v10
	v_sin_f32 v10, v10
	s_nop 1
	v_cvt_pk_bf16_f32 v11, v11, v10
	global_store_dword v[2:3], v11, off
	v_lshl_add_u64 v[2:3], v[2:3], 0, s[16:17]
	s_waitcnt vmcnt(31)
	v_cvt_f32_i32_e32 v10, v39
	v_mul_f32_e32 v10, v7, v10
	v_fract_f32_e32 v10, v10
	v_cos_f32 v11, v10
	v_sin_f32 v10, v10
	s_nop 1
	v_cvt_pk_bf16_f32 v11, v11, v10
	global_store_dword v[2:3], v11, off
	v_lshl_add_u64 v[2:3], v[2:3], 0, s[16:17]
	s_waitcnt vmcnt(31)
	v_cvt_f32_i32_e32 v10, v40
	v_mul_f32_e32 v10, v7, v10
	v_fract_f32_e32 v10, v10
	v_cos_f32 v11, v10
	v_sin_f32 v10, v10
	s_nop 1
	v_cvt_pk_bf16_f32 v11, v11, v10
	global_store_dword v[2:3], v11, off
	v_lshl_add_u64 v[2:3], v[2:3], 0, s[16:17]
	s_waitcnt vmcnt(31)
	v_cvt_f32_i32_e32 v10, v41
	v_mul_f32_e32 v10, v7, v10
	v_fract_f32_e32 v10, v10
	v_cos_f32 v11, v10
	v_sin_f32 v10, v10
	s_nop 1
	v_cvt_pk_bf16_f32 v11, v11, v10
	global_store_dword v[2:3], v11, off
	v_lshl_add_u64 v[2:3], v[2:3], 0, s[16:17]
	s_waitcnt vmcnt(31)
	v_cvt_f32_i32_e32 v10, v42
	v_mul_f32_e32 v10, v7, v10
	v_fract_f32_e32 v10, v10
	v_cos_f32 v11, v10
	v_sin_f32 v10, v10
	s_nop 1
	v_cvt_pk_bf16_f32 v11, v11, v10
	global_store_dword v[2:3], v11, off
	v_lshl_add_u64 v[2:3], v[2:3], 0, s[16:17]
	s_waitcnt vmcnt(31)
	v_cvt_f32_i32_e32 v10, v43
	v_mul_f32_e32 v10, v7, v10
	v_fract_f32_e32 v10, v10
	v_cos_f32 v11, v10
	v_sin_f32 v10, v10
	s_nop 1
	v_cvt_pk_bf16_f32 v11, v11, v10
	global_store_dword v[2:3], v11, off
	v_lshl_add_u64 v[2:3], v[2:3], 0, s[16:17]
	s_waitcnt vmcnt(31)
	v_cvt_f32_i32_e32 v10, v44
	v_mul_f32_e32 v10, v7, v10
	v_fract_f32_e32 v10, v10
	v_cos_f32 v11, v10
	v_sin_f32 v10, v10
	s_nop 1
	v_cvt_pk_bf16_f32 v11, v11, v10
	global_store_dword v[2:3], v11, off
	v_lshl_add_u64 v[2:3], v[2:3], 0, s[16:17]
	s_waitcnt vmcnt(31)
	v_cvt_f32_i32_e32 v10, v45
	v_mul_f32_e32 v10, v7, v10
	v_fract_f32_e32 v10, v10
	v_cos_f32 v11, v10
	v_sin_f32 v10, v10
	s_nop 1
	v_cvt_pk_bf16_f32 v11, v11, v10
	global_store_dword v[2:3], v11, off
	v_lshl_add_u64 v[2:3], v[2:3], 0, s[16:17]
	s_waitcnt vmcnt(31)
	v_cvt_f32_i32_e32 v10, v46
	v_mul_f32_e32 v10, v7, v10
	v_fract_f32_e32 v10, v10
	v_cos_f32 v11, v10
	v_sin_f32 v10, v10
	s_nop 1
	v_cvt_pk_bf16_f32 v11, v11, v10
	global_store_dword v[2:3], v11, off
	v_lshl_add_u64 v[2:3], v[2:3], 0, s[16:17]
	s_waitcnt vmcnt(31)
	v_cvt_f32_i32_e32 v10, v47
	v_mul_f32_e32 v10, v7, v10
	v_fract_f32_e32 v10, v10
	v_cos_f32 v11, v10
	v_sin_f32 v10, v10
	s_nop 1
	v_cvt_pk_bf16_f32 v11, v11, v10
	global_store_dword v[2:3], v11, off
	v_lshl_add_u64 v[2:3], v[2:3], 0, s[16:17]
	s_branch .LBB0_23
